# attention softmax: row max of the 80 scores as a 40-instruction v_max3 chain (was 162 max ops with per-operand canonicalisation)
# speedup vs baseline: 1.0146x; 1.0109x over previous
.LBB0_471:
	s_mov_b32 s4, 0xff800000
	v_cndmask_b32_e64 v70, v81, v226, s[78:79]
	v_max3_f32 v33, v18, v97, v20
	v_max3_f32 v33, v33, v19, v22
	v_max3_f32 v33, v33, v21, v24
	v_max3_f32 v33, v33, v23, v26
	v_max3_f32 v33, v33, v25, v28
	v_max3_f32 v33, v33, v27, v31
	v_max3_f32 v33, v33, v29, v30
	v_max3_f32 v33, v33, v32, v3
	v_max3_f32 v33, v33, v2, v5
	v_max3_f32 v33, v33, v4, v7
	v_max3_f32 v33, v33, v6, v9
	v_max3_f32 v33, v33, v8, v11
	v_max3_f32 v33, v33, v10, v13
	v_max3_f32 v33, v33, v12, v15
	v_max3_f32 v33, v33, v14, v17
	v_max3_f32 v33, v33, v16, v35
	v_max3_f32 v33, v33, v34, v37
	v_max3_f32 v33, v33, v36, v39
	v_max3_f32 v33, v33, v38, v41
	v_max3_f32 v33, v33, v40, v43
	v_max3_f32 v33, v33, v42, v45
	v_max3_f32 v33, v33, v44, v47
	v_max3_f32 v33, v33, v46, v49
	v_max3_f32 v33, v33, v48, v51
	v_max3_f32 v33, v33, v50, v53
	v_max3_f32 v33, v33, v52, v55
	v_max3_f32 v33, v33, v54, v57
	v_max3_f32 v33, v33, v56, v59
	v_max3_f32 v33, v33, v58, v61
	v_max3_f32 v33, v33, v60, v63
	v_max3_f32 v33, v33, v62, v65
	v_max3_f32 v33, v33, v64, v83
	v_max3_f32 v33, v33, v82, v85
	v_max3_f32 v33, v33, v84, v87
	v_max3_f32 v33, v33, v86, v89
	v_max3_f32 v33, v33, v88, v91
	v_max3_f32 v33, v33, v90, v93
	v_max3_f32 v33, v33, v92, v95
	v_max3_f32 v33, v33, v94, v70
	v_max_f32_e32 v33, v33, v96
	v_and_b32_e32 v67, 64, v209
	v_xor_b32_e32 v66, 32, v209
	v_add_u32_e32 v67, 64, v67
	v_cmp_lt_i32_e32 vcc, v66, v67
	s_nop 1
	v_cndmask_b32_e32 v66, v209, v66, vcc
	v_lshlrev_b32_e32 v118, 2, v66
	ds_bpermute_b32 v66, v118, v33
	s_waitcnt lgkmcnt(0)
	v_max_f32_e32 v66, v33, v66
	v_sub_f32_e32 v33, v97, v66
	v_exp_f32_e32 v33, v33
	v_sub_f32_e32 v18, v18, v66
	v_exp_f32_e32 v18, v18
	v_sub_f32_e32 v19, v19, v66
	v_exp_f32_e32 v19, v19
	v_sub_f32_e32 v20, v20, v66
	v_exp_f32_e32 v20, v20
	v_sub_f32_e32 v21, v21, v66
	v_add_f32_e32 v67, 0, v33
	v_exp_f32_e32 v21, v21
	v_sub_f32_e32 v22, v22, v66
	v_add_f32_e32 v67, v18, v67
	v_exp_f32_e32 v22, v22
	v_sub_f32_e32 v23, v23, v66
	v_add_f32_e32 v67, v19, v67
	v_exp_f32_e32 v23, v23
	v_sub_f32_e32 v24, v24, v66
	v_add_f32_e32 v67, v20, v67
	v_exp_f32_e32 v24, v24
	v_sub_f32_e32 v25, v25, v66
	v_add_f32_e32 v67, v21, v67
	v_exp_f32_e32 v119, v25
	v_sub_f32_e32 v25, v26, v66
	v_add_f32_e32 v67, v22, v67
	v_exp_f32_e32 v120, v25
	v_sub_f32_e32 v25, v27, v66
	v_add_f32_e32 v67, v23, v67
	v_exp_f32_e32 v121, v25
	v_sub_f32_e32 v26, v28, v66
	v_add_f32_e32 v25, v24, v67
	v_exp_f32_e32 v122, v26
	v_sub_f32_e32 v26, v29, v66
	v_add_f32_e32 v25, v119, v25
	v_exp_f32_e32 v123, v26
	v_sub_f32_e32 v26, v31, v66
	v_add_f32_e32 v25, v120, v25
	v_exp_f32_e32 v124, v26
	v_sub_f32_e32 v26, v32, v66
	v_add_f32_e32 v25, v121, v25
	v_exp_f32_e32 v125, v26
	v_sub_f32_e32 v26, v30, v66
	v_add_f32_e32 v25, v122, v25
	v_exp_f32_e32 v126, v26
	v_sub_f32_e32 v2, v2, v66
	v_add_f32_e32 v25, v123, v25
	v_exp_f32_e32 v103, v2
	v_sub_f32_e32 v2, v3, v66
	v_add_f32_e32 v25, v124, v25
	v_exp_f32_e32 v106, v2
	v_sub_f32_e32 v2, v4, v66
	v_add_f32_e32 v25, v125, v25
	v_exp_f32_e32 v107, v2
	v_sub_f32_e32 v3, v5, v66
	v_add_f32_e32 v2, v126, v25
	v_exp_f32_e32 v110, v3
	v_sub_f32_e32 v3, v6, v66
	v_add_f32_e32 v2, v103, v2
	v_exp_f32_e32 v111, v3
	v_sub_f32_e32 v3, v7, v66
	v_add_f32_e32 v2, v106, v2
	v_exp_f32_e32 v114, v3
	v_sub_f32_e32 v3, v8, v66
	v_add_f32_e32 v2, v107, v2
	v_exp_f32_e32 v115, v3
	v_sub_f32_e32 v3, v9, v66
	v_add_f32_e32 v2, v110, v2
	v_exp_f32_e32 v117, v3
	v_sub_f32_e32 v3, v10, v66
	v_add_f32_e32 v2, v111, v2
	v_exp_f32_e32 v102, v3
	v_sub_f32_e32 v3, v11, v66
	v_add_f32_e32 v2, v114, v2
	v_exp_f32_e32 v104, v3
	v_sub_f32_e32 v3, v12, v66
	v_add_f32_e32 v2, v115, v2
	v_exp_f32_e32 v105, v3
	v_sub_f32_e32 v3, v13, v66
	v_add_f32_e32 v2, v117, v2
	v_exp_f32_e32 v108, v3
	v_sub_f32_e32 v3, v14, v66
	v_add_f32_e32 v2, v102, v2
	v_exp_f32_e32 v109, v3
	v_sub_f32_e32 v3, v15, v66
	v_add_f32_e32 v2, v104, v2
	v_exp_f32_e32 v112, v3
	v_sub_f32_e32 v3, v16, v66
	v_add_f32_e32 v2, v105, v2
	v_exp_f32_e32 v113, v3
	v_sub_f32_e32 v3, v17, v66
	v_add_f32_e32 v2, v108, v2
	v_exp_f32_e32 v116, v3
	v_sub_f32_e32 v3, v34, v66
	v_add_f32_e32 v2, v109, v2
	v_exp_f32_e32 v72, v3
	v_sub_f32_e32 v3, v35, v66
	v_add_f32_e32 v2, v112, v2
	v_exp_f32_e32 v75, v3
	v_sub_f32_e32 v3, v36, v66
	v_add_f32_e32 v2, v113, v2
	v_exp_f32_e32 v76, v3
	v_sub_f32_e32 v3, v37, v66
	v_add_f32_e32 v2, v116, v2
	v_exp_f32_e32 v79, v3
	v_sub_f32_e32 v3, v38, v66
	v_add_f32_e32 v2, v72, v2
	v_exp_f32_e32 v80, v3
	v_sub_f32_e32 v3, v39, v66
	v_add_f32_e32 v2, v75, v2
	v_exp_f32_e32 v98, v3
	v_sub_f32_e32 v3, v40, v66
	v_add_f32_e32 v2, v76, v2
	v_exp_f32_e32 v99, v3
	v_sub_f32_e32 v3, v41, v66
	v_add_f32_e32 v2, v79, v2
	v_exp_f32_e32 v101, v3
	v_sub_f32_e32 v3, v42, v66
	v_add_f32_e32 v2, v80, v2
	v_exp_f32_e32 v71, v3
	v_sub_f32_e32 v3, v43, v66
	v_add_f32_e32 v2, v98, v2
	v_exp_f32_e32 v73, v3
	v_sub_f32_e32 v3, v44, v66
	v_add_f32_e32 v2, v99, v2
	v_exp_f32_e32 v74, v3
	v_sub_f32_e32 v3, v45, v66
	v_add_f32_e32 v2, v101, v2
	v_exp_f32_e32 v77, v3
	v_sub_f32_e32 v3, v46, v66
	v_add_f32_e32 v2, v71, v2
	v_exp_f32_e32 v78, v3
	v_sub_f32_e32 v3, v47, v66
	v_add_f32_e32 v2, v73, v2
	v_exp_f32_e32 v81, v3
	v_sub_f32_e32 v3, v48, v66
	v_add_f32_e32 v2, v74, v2
	v_exp_f32_e32 v97, v3
	v_sub_f32_e32 v3, v49, v66
	v_add_f32_e32 v2, v77, v2
	v_exp_f32_e32 v100, v3
	v_sub_f32_e32 v3, v50, v66
	v_add_f32_e32 v2, v78, v2
	v_exp_f32_e32 v41, v3
	v_sub_f32_e32 v3, v51, v66
	v_add_f32_e32 v2, v81, v2
	v_exp_f32_e32 v46, v3
	v_sub_f32_e32 v3, v52, v66
	v_add_f32_e32 v2, v97, v2
	v_exp_f32_e32 v47, v3
	v_sub_f32_e32 v3, v53, v66
	v_add_f32_e32 v2, v100, v2
	v_exp_f32_e32 v53, v3
	v_sub_f32_e32 v3, v54, v66
	v_add_f32_e32 v2, v41, v2
	v_exp_f32_e32 v54, v3
	v_sub_f32_e32 v3, v55, v66
	v_add_f32_e32 v2, v46, v2
	v_exp_f32_e32 v67, v3
	v_sub_f32_e32 v3, v56, v66
	v_add_f32_e32 v2, v47, v2
	v_exp_f32_e32 v68, v3
	v_sub_f32_e32 v3, v57, v66
	v_add_f32_e32 v2, v53, v2
	v_exp_f32_e32 v69, v3
	v_sub_f32_e32 v3, v58, v66
	v_add_f32_e32 v2, v54, v2
	v_exp_f32_e32 v38, v3
	v_sub_f32_e32 v3, v59, v66
	v_add_f32_e32 v2, v67, v2
	v_exp_f32_e32 v44, v3
	v_sub_f32_e32 v3, v60, v66
	v_add_f32_e32 v2, v68, v2
	v_exp_f32_e32 v45, v3
	v_sub_f32_e32 v3, v61, v66
	v_add_f32_e32 v2, v69, v2
	v_exp_f32_e32 v51, v3
	v_sub_f32_e32 v3, v62, v66
	v_add_f32_e32 v2, v38, v2
	v_exp_f32_e32 v52, v3
	v_sub_f32_e32 v3, v63, v66
	v_add_f32_e32 v2, v44, v2
	v_exp_f32_e32 v57, v3
	v_sub_f32_e32 v3, v64, v66
	v_add_f32_e32 v2, v45, v2
	v_exp_f32_e32 v58, v3
	v_sub_f32_e32 v3, v65, v66
	v_add_f32_e32 v2, v51, v2
	v_exp_f32_e32 v62, v3
	v_sub_f32_e32 v3, v82, v66
	v_add_f32_e32 v2, v52, v2
	v_exp_f32_e32 v37, v3
	v_sub_f32_e32 v3, v83, v66
	v_add_f32_e32 v2, v57, v2
	v_exp_f32_e32 v42, v3
	v_sub_f32_e32 v3, v84, v66
	v_add_f32_e32 v2, v58, v2
	v_exp_f32_e32 v43, v3
	v_sub_f32_e32 v3, v85, v66
	v_add_f32_e32 v2, v62, v2
	v_exp_f32_e32 v49, v3
	v_sub_f32_e32 v3, v86, v66
	v_add_f32_e32 v2, v37, v2
	v_exp_f32_e32 v50, v3
	v_sub_f32_e32 v3, v87, v66
	v_add_f32_e32 v2, v42, v2
	v_exp_f32_e32 v55, v3
	v_sub_f32_e32 v3, v88, v66
	v_add_f32_e32 v2, v43, v2
	v_exp_f32_e32 v56, v3
	v_sub_f32_e32 v3, v89, v66
	v_add_f32_e32 v2, v49, v2
	v_exp_f32_e32 v61, v3
	v_sub_f32_e32 v3, v90, v66
	v_add_f32_e32 v2, v50, v2
	v_exp_f32_e32 v36, v3
	v_sub_f32_e32 v3, v91, v66
	v_add_f32_e32 v2, v55, v2
	v_exp_f32_e32 v39, v3
	v_sub_f32_e32 v3, v92, v66
	v_add_f32_e32 v2, v56, v2
	v_exp_f32_e32 v40, v3
	v_add_f32_e32 v2, v61, v2
	v_add_f32_e32 v2, v36, v2
	v_add_f32_e32 v2, v39, v2
	v_add_f32_e32 v14, v40, v2
	v_sub_f32_e32 v2, v93, v66
	v_exp_f32_e32 v48, v2
	v_cvt_pk_bf16_f32 v2, v33, v18
	v_cvt_pk_bf16_f32 v3, v19, v20
	v_cvt_pk_bf16_f32 v4, v21, v22
	v_cvt_pk_bf16_f32 v5, v23, v24
	s_bitcmp1_b32 s96, 0
	s_cbranch_scc1 .Latt_b3m
	s_waitcnt vmcnt(0)
